# attention tile loop: next tile's K (LDS-DMA) / V requests moved from the tile head into the shadow of the first score MFMAs; their address arithmetic made scalar-only (lane parts hoisted out of the lo
# baseline (speedup 1.0000x reference)
.LBB0_438:
	s_lshl_b32 s2, s12, 1
	s_and_b32 s2, s2, 14
	s_ashr_i32 s3, s12, 7
	s_add_i32 s2, s2, s3
	s_ashr_i32 s3, s2, 2
	s_lshl_b32 s22, s3, 8
	s_lshl_b32 s21, s3, 12
	s_lshl_b32 s3, s12, 5
	s_lshl_b32 s2, s2, 7
	v_mov_b32_e32 v205, v3
	v_readlane_b32 s8, v254, 27
	s_and_b32 s3, s3, 0xf00
	s_and_b32 s10, s2, 0x180
	v_mbcnt_lo_u32_b32 v0, -1, 0
	v_mbcnt_hi_u32_b32 v0, -1, v0
	s_add_i32 s13, s22, 0x4000
	v_add_u32_e32 v204, s8, v0
	s_or_b32 s11, s21, s3
	s_lshl_b32 s80, s10, 1
	s_add_u32 s2, s52, s80
	v_lshlrev_b32_e32 v0, 4, v204
	v_add_u32_e32 v6, 0x200, v204
	v_add_u32_e32 v12, 0x400, v204
	v_add_u32_e32 v14, 0x600, v204
	s_addc_u32 s3, s53, 0
	v_and_b32_e32 v2, 0xf0, v0
	v_ashrrev_i32_e32 v36, 4, v204
	v_ashrrev_i32_e32 v38, 4, v6
	v_ashrrev_i32_e32 v40, 4, v12
	v_ashrrev_i32_e32 v42, 4, v14
	v_add_u32_e32 v20, 0x800, v204
	v_add_u32_e32 v22, 0xa00, v204
	v_lshl_add_u64 v[0:1], s[2:3], 0, v[2:3]
	v_add_u32_e32 v4, s11, v36
	s_movk_i32 s18, 0x1400
	v_add_u32_e32 v6, s11, v38
	v_add_u32_e32 v12, s11, v40
	v_add_u32_e32 v14, s11, v42
	v_ashrrev_i32_e32 v44, 4, v20
	v_ashrrev_i32_e32 v46, 4, v22
	v_add_u32_e32 v28, 0xc00, v204
	v_add_u32_e32 v32, 0xe00, v204
	v_mad_i64_i32 v[4:5], s[8:9], v4, s18, v[0:1]
	v_mad_i64_i32 v[8:9], s[8:9], v6, s18, v[0:1]
	v_mad_i64_i32 v[12:13], s[8:9], v12, s18, v[0:1]
	v_mad_i64_i32 v[16:17], s[8:9], v14, s18, v[0:1]
	v_add_u32_e32 v20, s11, v44
	v_add_u32_e32 v22, s11, v46
	v_ashrrev_i32_e32 v47, 4, v28
	v_ashrrev_i32_e32 v48, 4, v32
	global_load_dwordx4 v[4:7], v[4:5], off
	s_nop 0
	global_load_dwordx4 v[8:11], v[8:9], off
	s_nop 0
	global_load_dwordx4 v[12:15], v[12:13], off
	s_nop 0
	global_load_dwordx4 v[16:19], v[16:17], off
	v_mad_i64_i32 v[20:21], s[8:9], v20, s18, v[0:1]
	v_mad_i64_i32 v[24:25], s[8:9], v22, s18, v[0:1]
	v_add_u32_e32 v28, s11, v47
	v_add_u32_e32 v32, s11, v48
	global_load_dwordx4 v[20:23], v[20:21], off
	s_nop 0
	global_load_dwordx4 v[24:27], v[24:25], off
	v_mad_i64_i32 v[28:29], s[8:9], v28, s18, v[0:1]
	v_mad_i64_i32 v[0:1], s[8:9], v32, s18, v[0:1]
	global_load_dwordx4 v[28:31], v[28:29], off
	v_add_u32_e32 v206, 0x11800, v205
	global_load_dwordx4 v[32:35], v[0:1], off
	v_add_u32_e32 v0, v206, v2
	v_mad_u64_u32 v[36:37], s[14:15], v36, s30, v[0:1]
	v_mad_u64_u32 v[38:39], s[14:15], v38, s30, v[0:1]
	v_mad_u64_u32 v[40:41], s[14:15], v40, s30, v[0:1]
	v_mad_u64_u32 v[42:43], s[14:15], v42, s30, v[0:1]
	v_mad_u64_u32 v[44:45], s[14:15], v44, s30, v[0:1]
	v_and_b32_e32 v2, 63, v204
	v_ashrrev_i32_e32 v49, 6, v204
	s_mov_b64 s[24:25], 0x400
	v_readfirstlane_b32 s8, v49
	s_mov_b32 s23, 0
	v_mov_b32_e32 v210, 0
	v_mov_b32_e32 v208, 0xf149f2ca
	v_mov_b32_e32 v209, 0xf149f2ca
	v_mov_b32_e32 v207, 0
	s_waitcnt vmcnt(7)
	ds_write_b128 v36, v[4:7]
	s_waitcnt vmcnt(6)
	ds_write_b128 v38, v[8:11]
	s_waitcnt vmcnt(5)
	ds_write_b128 v40, v[12:15]
	s_waitcnt vmcnt(4)
	ds_write_b128 v42, v[16:19]
	s_waitcnt vmcnt(3)
	ds_write_b128 v44, v[20:23]
	v_mad_u64_u32 v[4:5], s[14:15], v46, s30, v[0:1]
	s_waitcnt vmcnt(2)
	ds_write_b128 v4, v[24:27]
	v_mad_u64_u32 v[4:5], s[14:15], v47, s30, v[0:1]
	v_mad_u64_u32 v[0:1], s[14:15], v48, s30, v[0:1]
	s_waitcnt vmcnt(1)
	ds_write_b128 v4, v[28:31]
	s_waitcnt vmcnt(0)
	ds_write_b128 v0, v[32:35]
	v_or_b32_e32 v4, s13, v2
	v_mov_b64_e32 v[0:1], s[52:53]
	v_mad_i64_i32 v[0:1], s[14:15], v4, s18, v[0:1]
	s_lshl_b32 s14, s8, 3
	s_add_i32 s15, s21, 0xffffff00
	s_cmp_lt_i32 s8, 32
	s_cselect_b32 s9, s13, s15
	s_add_i32 s9, s9, s14
	s_mul_hi_i32 s18, s9, 0x1400
	s_mulk_i32 s9, 0x1400
	s_add_u32 s9, s52, s9
	v_lshlrev_b32_e32 v4, 3, v49
	s_addc_u32 s19, s53, s18
	v_lshl_add_u64 v[0:1], v[0:1], 0, s[80:81]
	v_ashrrev_i32_e32 v5, 31, v4
	s_add_u32 s18, s9, s80
	v_lshl_add_u64 v[0:1], v[4:5], 1, v[0:1]
	s_addc_u32 s19, s19, 0
	v_lshlrev_b32_e32 v2, 2, v2
	global_load_dwordx4 v[176:179], v[0:1], off offset:2048
	global_load_dwordx4 v[180:183], v[0:1], off offset:2176
	v_lshl_add_u64 v[0:1], s[18:19], 0, v[2:3]
	s_mul_i32 s19, s8, 0x880
	v_add_u32_e32 v4, s19, v205
	s_or_b32 s20, s14, 1
	v_readfirstlane_b32 s9, v4
	s_cmpk_lt_i32 s20, 0x100
	s_mov_b32 m0, s9
	s_cselect_b32 s9, s13, s15
	s_add_i32 s9, s9, s20
	s_mul_hi_i32 s18, s9, 0x1400
	s_mulk_i32 s9, 0x1400
	s_add_u32 s9, s52, s9
	s_mulk_i32 s20, 0x110
	s_addc_u32 s18, s53, s18
	v_add_u32_e32 v4, s20, v205
	v_lshl_add_u64 v[0:1], v[0:1], 0, s[24:25]
	s_add_u32 s26, s9, s80
	v_readfirstlane_b32 s9, v4
	global_load_lds_dword v[0:1], off
	s_addc_u32 s27, s18, 0
	s_mov_b32 m0, s9
	s_or_b32 s9, s14, 2
	s_cmpk_lt_i32 s9, 0x100
	s_cselect_b32 s18, s13, s15
	s_add_i32 s9, s18, s9
	s_mul_hi_i32 s18, s9, 0x1400
	s_mulk_i32 s9, 0x1400
	s_add_u32 s9, s52, s9
	s_addc_u32 s18, s53, s18
	v_lshl_add_u64 v[0:1], s[26:27], 0, v[2:3]
	s_add_u32 s26, s9, s80
	s_addc_u32 s27, s18, 0
	s_add_i32 s9, s20, 0x110
	v_add_u32_e32 v4, s9, v205
	v_lshl_add_u64 v[0:1], v[0:1], 0, s[24:25]
	v_readfirstlane_b32 s9, v4
	global_load_lds_dword v[0:1], off
	s_mov_b32 m0, s9
	s_or_b32 s9, s14, 3
	s_cmpk_lt_i32 s9, 0x100
	s_cselect_b32 s18, s13, s15
	s_add_i32 s9, s18, s9
	s_mul_hi_i32 s18, s9, 0x1400
	s_mulk_i32 s9, 0x1400
	s_add_u32 s9, s52, s9
	s_addc_u32 s18, s53, s18
	v_lshl_add_u64 v[0:1], s[26:27], 0, v[2:3]
	s_add_u32 s26, s9, s80
	s_addc_u32 s27, s18, 0
	s_add_i32 s9, s20, 0x220
	v_add_u32_e32 v4, s9, v205
	v_lshl_add_u64 v[0:1], v[0:1], 0, s[24:25]
	v_readfirstlane_b32 s9, v4
	global_load_lds_dword v[0:1], off
	s_mov_b32 m0, s9
	s_or_b32 s9, s14, 4
	s_cmpk_lt_i32 s9, 0x100
	s_cselect_b32 s18, s13, s15
	s_add_i32 s9, s18, s9
	s_mul_hi_i32 s18, s9, 0x1400
	s_mulk_i32 s9, 0x1400
	s_add_u32 s9, s52, s9
	s_addc_u32 s18, s53, s18
	v_lshl_add_u64 v[0:1], s[26:27], 0, v[2:3]
	s_add_u32 s26, s9, s80
	s_addc_u32 s27, s18, 0
	s_add_i32 s9, s20, 0x330
	v_add_u32_e32 v4, s9, v205
	v_lshl_add_u64 v[0:1], v[0:1], 0, s[24:25]
	v_readfirstlane_b32 s9, v4
	global_load_lds_dword v[0:1], off
	s_mov_b32 m0, s9
	s_or_b32 s9, s14, 5
	s_cmpk_lt_i32 s9, 0x100
	s_cselect_b32 s18, s13, s15
	s_add_i32 s9, s18, s9
	s_mul_hi_i32 s18, s9, 0x1400
	s_mulk_i32 s9, 0x1400
	s_add_u32 s9, s52, s9
	s_addc_u32 s18, s53, s18
	v_lshl_add_u64 v[0:1], s[26:27], 0, v[2:3]
	s_add_u32 s26, s9, s80
	s_addc_u32 s27, s18, 0
	s_add_i32 s9, s20, 0x440
	v_add_u32_e32 v4, s9, v205
	v_lshl_add_u64 v[0:1], v[0:1], 0, s[24:25]
	v_readfirstlane_b32 s9, v4
	global_load_lds_dword v[0:1], off
	s_mov_b32 m0, s9
	s_or_b32 s9, s14, 6
	s_cmpk_lt_i32 s9, 0x100
	s_cselect_b32 s18, s13, s15
	s_add_i32 s9, s18, s9
	s_mul_hi_i32 s18, s9, 0x1400
	s_mulk_i32 s9, 0x1400
	s_add_u32 s9, s52, s9
	s_addc_u32 s18, s53, s18
	v_lshl_add_u64 v[0:1], s[26:27], 0, v[2:3]
	s_add_u32 s26, s9, s80
	s_addc_u32 s27, s18, 0
	s_add_i32 s9, s20, 0x550
	v_add_u32_e32 v4, s9, v205
	v_lshl_add_u64 v[0:1], v[0:1], 0, s[24:25]
	v_readfirstlane_b32 s9, v4
	global_load_lds_dword v[0:1], off
	s_mov_b32 m0, s9
	s_or_b32 s9, s14, 7
	s_cmpk_lt_i32 s9, 0x100
	s_cselect_b32 s18, s13, s15
	s_add_i32 s9, s18, s9
	s_mul_hi_i32 s18, s9, 0x1400
	s_mulk_i32 s9, 0x1400
	s_add_u32 s9, s52, s9
	s_addc_u32 s18, s53, s18
	v_lshl_add_u64 v[0:1], s[26:27], 0, v[2:3]
	s_add_u32 s26, s9, s80
	v_lshl_add_u64 v[0:1], v[0:1], 0, s[24:25]
	s_addc_u32 s27, s18, 0
	s_add_i32 s9, s20, 0x660
	global_load_lds_dword v[0:1], off
	v_lshl_add_u64 v[0:1], s[26:27], 0, v[2:3]
	v_add_u32_e32 v2, s9, v205
	v_lshl_add_u64 v[0:1], v[0:1], 0, s[24:25]
	v_readfirstlane_b32 s9, v2
	s_mov_b32 m0, s9
	s_movk_i32 s9, 0x480
	global_load_lds_dword v[0:1], off
	v_bfe_u32 v0, v204, 2, 2
	v_and_b32_e32 v1, 12, v204
	v_cmp_ne_u32_e32 vcc, 2, v0
	v_mov_b32_e32 v14, v3
	v_mov_b32_e32 v15, v3
	v_cndmask_b32_e32 v1, 4, v1, vcc
	v_cmp_ne_u32_e32 vcc, 1, v0
	v_mov_b32_e32 v2, v3
	v_mov_b32_e32 v4, v3
	v_cndmask_b32_e32 v0, 8, v1, vcc
	v_and_or_b32 v0, v204, 51, v0
	v_mul_lo_u32 v1, v49, s9
	v_lshlrev_b32_e32 v0, 1, v0
	v_add3_u32 v0, v205, v1, v0
	s_waitcnt vmcnt(0)
	ds_write_b16 v0, v176 offset:34816
	ds_write_b16_d16_hi v0, v176 offset:34960
	ds_write_b16 v0, v177 offset:35104
	ds_write_b16_d16_hi v0, v177 offset:35248
	ds_write_b16 v0, v178 offset:35392
	ds_write_b16_d16_hi v0, v178 offset:35536
	ds_write_b16 v0, v179 offset:35680
	ds_write_b16_d16_hi v0, v179 offset:35824
	ds_write_b16 v0, v180 offset:44032
	ds_write_b16_d16_hi v0, v180 offset:44176
	ds_write_b16 v0, v181 offset:44320
	ds_write_b16_d16_hi v0, v181 offset:44464
	ds_write_b16 v0, v182 offset:44608
	ds_write_b16_d16_hi v0, v182 offset:44752
	ds_write_b16 v0, v183 offset:44896
	ds_write_b16_d16_hi v0, v183 offset:45040
	v_mov_b32_e32 v0, v3
	v_mov_b32_e32 v1, v3
	v_mov_b32_e32 v5, v3
	v_mov_b32_e32 v6, v3
	v_mov_b32_e32 v7, v3
	v_mov_b32_e32 v8, v3
	v_mov_b32_e32 v9, v3
	v_mov_b32_e32 v10, v3
	v_mov_b32_e32 v11, v3
	v_mov_b32_e32 v12, v3
	v_mov_b32_e32 v13, v3
	v_mov_b64_e32 v[30:31], v[14:15]
	v_mov_b64_e32 v[62:63], v[14:15]
	v_mov_b64_e32 v[94:95], v[14:15]
	v_mov_b64_e32 v[126:127], v[14:15]
	v_mov_b64_e32 v[46:47], v[14:15]
	v_mov_b64_e32 v[78:79], v[14:15]
	v_mov_b64_e32 v[110:111], v[14:15]
	v_mov_b64_e32 v[142:143], v[14:15]
	s_lshl_b32 s18, s8, 5
	s_addk_i32 s21, 0xff40
	s_addk_i32 s22, 0x4040
	v_mov_b64_e32 v[28:29], v[12:13]
	v_mov_b64_e32 v[26:27], v[10:11]
	v_mov_b64_e32 v[24:25], v[8:9]
	v_mov_b64_e32 v[22:23], v[6:7]
	v_mov_b64_e32 v[20:21], v[4:5]
	v_mov_b64_e32 v[18:19], v[2:3]
	v_mov_b64_e32 v[16:17], v[0:1]
	v_mov_b64_e32 v[60:61], v[12:13]
	v_mov_b64_e32 v[58:59], v[10:11]
	v_mov_b64_e32 v[56:57], v[8:9]
	v_mov_b64_e32 v[54:55], v[6:7]
	v_mov_b64_e32 v[52:53], v[4:5]
	v_mov_b64_e32 v[50:51], v[2:3]
	v_mov_b64_e32 v[48:49], v[0:1]
	v_mov_b64_e32 v[92:93], v[12:13]
	v_mov_b64_e32 v[90:91], v[10:11]
	v_mov_b64_e32 v[88:89], v[8:9]
	v_mov_b64_e32 v[86:87], v[6:7]
	v_mov_b64_e32 v[84:85], v[4:5]
	v_mov_b64_e32 v[82:83], v[2:3]
	v_mov_b64_e32 v[80:81], v[0:1]
	v_mov_b64_e32 v[124:125], v[12:13]
	v_mov_b64_e32 v[122:123], v[10:11]
	v_mov_b64_e32 v[120:121], v[8:9]
	v_mov_b64_e32 v[118:119], v[6:7]
	v_mov_b64_e32 v[116:117], v[4:5]
	v_mov_b64_e32 v[114:115], v[2:3]
	v_mov_b64_e32 v[112:113], v[0:1]
	v_mov_b64_e32 v[44:45], v[12:13]
	v_mov_b64_e32 v[42:43], v[10:11]
	v_mov_b64_e32 v[40:41], v[8:9]
	v_mov_b64_e32 v[38:39], v[6:7]
	v_mov_b64_e32 v[36:37], v[4:5]
	v_mov_b64_e32 v[34:35], v[2:3]
	v_mov_b64_e32 v[32:33], v[0:1]
	v_mov_b64_e32 v[76:77], v[12:13]
	v_mov_b64_e32 v[74:75], v[10:11]
	v_mov_b64_e32 v[72:73], v[8:9]
	v_mov_b64_e32 v[70:71], v[6:7]
	v_mov_b64_e32 v[68:69], v[4:5]
	v_mov_b64_e32 v[66:67], v[2:3]
	v_mov_b64_e32 v[64:65], v[0:1]
	v_mov_b64_e32 v[108:109], v[12:13]
	v_mov_b64_e32 v[106:107], v[10:11]
	v_mov_b64_e32 v[104:105], v[8:9]
	v_mov_b64_e32 v[102:103], v[6:7]
	v_mov_b64_e32 v[100:101], v[4:5]
	v_mov_b64_e32 v[98:99], v[2:3]
	v_mov_b64_e32 v[96:97], v[0:1]
	v_mov_b64_e32 v[140:141], v[12:13]
	v_mov_b64_e32 v[138:139], v[10:11]
	v_mov_b64_e32 v[136:137], v[8:9]
	v_mov_b64_e32 v[134:135], v[6:7]
	v_mov_b64_e32 v[132:133], v[4:5]
	v_mov_b64_e32 v[130:131], v[2:3]
	v_mov_b64_e32 v[128:129], v[0:1]
	s_mov_b32 s26, 0
	s_waitcnt lgkmcnt(0)
	s_barrier
	v_and_b32_e32 v2, 31, v204
	v_bfe_u32 v15, v204, 5, 1
	v_lshlrev_b32_e32 v15, 4, v15
	v_or_b32_e32 v13, s18, v2
	v_mul_u32_u24_e32 v1, 0x90, v2
	v_mad_u32_u24 v0, v2, s30, v15
	v_mul_lo_u32 v13, v13, s30
	v_add_u32_e32 v0, v0, v205
	v_add3_u32 v1, v1, v15, v205
	v_add3_u32 v13, v206, v13, v15
	v_bfe_u32 v15, v204, 2, 2
	v_and_b32_e32 v2, 12, v204
	v_cmp_ne_u32_e32 vcc, 2, v15
	s_movk_i32 s8, 0x480
	v_ashrrev_i32_e32 v211, 6, v204
	v_cndmask_b32_e32 v2, 4, v2, vcc
	v_cmp_ne_u32_e32 vcc, 1, v15
	v_mul_lo_u32 v211, v211, s8
	s_nop 0
	v_cndmask_b32_e32 v15, 8, v2, vcc
	v_and_or_b32 v2, v204, 51, v15
	v_lshlrev_b32_e32 v2, 1, v2
	v_add3_u32 v2, v205, v211, v2
	v_and_b32_e32 v206, 63, v204
	v_ashrrev_i32_e32 v252, 6, v204
	s_movk_i32 s8, 0x1400
	v_lshlrev_b32_e32 v252, 4, v252
	v_mad_u32_u24 v252, v206, s8, v252
	v_lshlrev_b32_e32 v206, 2, v206
	v_add_u32_e32 v206, 0x400, v206
.LBB0_439:
	s_add_i32 s25, s26, 1
	s_and_b32 s27, s26, 1
	s_mul_i32 s24, s27, 0x4400
	s_mul_i32 s31, s27, 0x4800
	v_add_u32_e32 v12, s24, v0
	v_add_u32_e32 v14, s31, v1
	ds_read_b128 v[228:231], v12 offset:0
	ds_read_b128 v[232:235], v12 offset:32
	ds_read_b128 v[236:239], v12 offset:64
	ds_read_b128 v[240:243], v12 offset:96
	ds_read_b128 v[244:247], v13 offset:0
	ds_read_b128 v[248:251], v13 offset:32
	ds_read_b128 v[4:7], v13 offset:64
	ds_read_b128 v[8:11], v13 offset:96
	ds_read_b128 v[184:187], v14 offset:34816
	ds_read_b128 v[188:191], v14 offset:39424
	ds_read_b128 v[192:195], v14 offset:44032
	ds_read_b128 v[196:199], v14 offset:48640
	ds_read_b128 v[200:203], v14 offset:34848
	ds_read_b128 v[212:215], v14 offset:39456
	ds_read_b128 v[216:219], v14 offset:44064
	s_cmpk_gt_u32 s26, 0x42
	s_waitcnt lgkmcnt(7)
	ds_read_b128 v[220:223], v14 offset:48672
	s_cbranch_scc1 .Lat_noload
	v_mfma_f32_32x32x16_bf16 v[144:159], v[228:231], v[244:247], 0
	s_cmp_lt_u32 s26, 3
	s_cselect_b32 s24, s22, s21
	s_cselect_b32 s31, s13, s15
	s_add_i32 s24, s24, s23
	s_add_i32 s31, s31, s14
	s_mul_hi_i32 s37, s24, 0x1400
	s_mul_i32 s36, s24, 0x1400
	s_add_i32 s31, s31, s23
	s_add_u32 s36, s2, s36
	s_addc_u32 s37, s3, s37
	s_add_i32 s31, s31, 64
	global_load_dwordx4 v[176:179], v252, s[36:37] offset:2048
	global_load_dwordx4 v[180:183], v252, s[36:37] offset:2176
	s_mul_hi_i32 s37, s31, 0x1400
	s_mul_i32 s36, s31, 0x1400
	s_add_u32 s36, s2, s36
	v_mfma_f32_32x32x16_bf16 v[144:159], v[232:235], v[248:251], v[144:159]
	s_addc_u32 s37, s3, s37
	v_readfirstlane_b32 s38, v205
	s_xor_b32 s39, s27, 1
	s_mul_i32 s39, s39, 0x4400
	s_add_i32 s38, s38, s19
	s_add_i32 s38, s38, s39
	s_add_i32 m0, s38, 0
	s_nop 0
	global_load_lds_dword v206, s[36:37]
	s_add_u32 s36, s36, 0x1400
	s_addc_u32 s37, s37, 0
	s_add_i32 m0, s38, 272
	s_nop 0
	global_load_lds_dword v206, s[36:37]
	s_add_u32 s36, s36, 0x1400
	v_mfma_f32_32x32x16_bf16 v[144:159], v[236:239], v[4:7], v[144:159]
	s_addc_u32 s37, s37, 0
	s_add_i32 m0, s38, 544
	s_nop 0
	global_load_lds_dword v206, s[36:37]
	s_add_u32 s36, s36, 0x1400
	s_addc_u32 s37, s37, 0
	s_add_i32 m0, s38, 816
	s_nop 0
	global_load_lds_dword v206, s[36:37]
	s_add_u32 s36, s36, 0x1400
	s_addc_u32 s37, s37, 0
	s_add_i32 m0, s38, 1088
	s_nop 0
	global_load_lds_dword v206, s[36:37]
	s_add_u32 s36, s36, 0x1400
	v_mfma_f32_32x32x16_bf16 v[144:159], v[240:243], v[8:11], v[144:159]
	s_addc_u32 s37, s37, 0
	s_add_i32 m0, s38, 1360
	s_nop 0
	global_load_lds_dword v206, s[36:37]
	s_add_u32 s36, s36, 0x1400
	s_addc_u32 s37, s37, 0
	s_add_i32 m0, s38, 1632
	s_nop 0
	global_load_lds_dword v206, s[36:37]
	s_add_u32 s36, s36, 0x1400
	s_addc_u32 s37, s37, 0
	s_add_i32 m0, s38, 1904
	s_nop 0
	global_load_lds_dword v206, s[36:37]
	s_branch .Lat_join
.Lat_noload:
	v_mfma_f32_32x32x16_bf16 v[144:159], v[228:231], v[244:247], 0
	v_mfma_f32_32x32x16_bf16 v[144:159], v[232:235], v[248:251], v[144:159]
	v_mfma_f32_32x32x16_bf16 v[144:159], v[236:239], v[4:7], v[144:159]
	v_mfma_f32_32x32x16_bf16 v[144:159], v[240:243], v[8:11], v[144:159]
.Lat_join:
	s_waitcnt lgkmcnt(0)
	ds_read_b128 v[228:231], v12 offset:128
	ds_read_b128 v[232:235], v12 offset:160
	ds_read_b128 v[236:239], v12 offset:192
	ds_read_b128 v[240:243], v12 offset:224
	ds_read_b128 v[244:247], v13 offset:128
	ds_read_b128 v[248:251], v13 offset:160
	ds_read_b128 v[4:7], v13 offset:192
	ds_read_b128 v[8:11], v13 offset:224
	s_nop 3
	v_max3_f32 v15, v144, v145, v146
	v_max3_f32 v211, v147, v148, v149
	v_max3_f32 v224, v150, v151, v152
	v_max3_f32 v225, v153, v154, v155
	v_max3_f32 v227, v156, v157, v158
	v_max3_f32 v15, v15, v211, v159
	v_max3_f32 v224, v224, v225, v227
	v_max_f32_e32 v15, v15, v224
	v_mov_b32_e32 v211, v15
	v_add_f32_e32 v225, 0x41000000, v209
	s_nop 1
	v_permlane32_swap_b32_e32 v15, v211
	v_max_f32_e32 v15, v15, v211
	v_cmp_gt_f32_e32 vcc, v15, v225
	s_cbranch_vccnz .Lat_slow0_s0

.LBB0_745:
	s_and_b64 vcc, exec, s[0:1]
	s_cbranch_vccz .LBB0_454
	s_ashr_i32 s0, s22, 2
	s_lshl_b32 s15, s0, 8
	s_lshl_b32 s12, s0, 12
	s_lshl_b32 s0, s22, 7
	v_mov_b32_e32 v205, v3
	v_readlane_b32 s1, v254, 27
	s_and_b32 s8, s0, 0x180
	v_mbcnt_lo_u32_b32 v0, -1, 0
	v_mbcnt_hi_u32_b32 v0, -1, v0
	s_add_i32 s9, s15, 0x4000
	v_add_u32_e32 v204, s1, v0
	s_lshl_b32 s80, s8, 1
	s_add_u32 s0, s52, s80
	v_lshlrev_b32_e32 v0, 4, v204
	v_add_u32_e32 v6, 0x200, v204
	v_add_u32_e32 v12, 0x400, v204
	v_add_u32_e32 v14, 0x600, v204
	v_add_u32_e32 v20, 0x800, v204
	v_add_u32_e32 v22, 0xa00, v204
	v_add_u32_e32 v28, 0xc00, v204
	v_add_u32_e32 v32, 0xe00, v204
	s_addc_u32 s1, s53, 0
	v_and_b32_e32 v2, 0xf0, v0
	v_ashrrev_i32_e32 v36, 4, v204
	v_ashrrev_i32_e32 v38, 4, v6
	v_ashrrev_i32_e32 v40, 4, v12
	v_ashrrev_i32_e32 v42, 4, v14
	v_ashrrev_i32_e32 v44, 4, v20
	v_ashrrev_i32_e32 v46, 4, v22
	v_ashrrev_i32_e32 v48, 4, v28
	v_ashrrev_i32_e32 v50, 4, v32
	v_lshl_add_u64 v[0:1], s[0:1], 0, v[2:3]
	v_add_u32_e32 v4, s9, v36
	s_movk_i32 s13, 0x1400
	v_add_u32_e32 v6, s9, v38
	v_add_u32_e32 v12, s9, v40
	v_add_u32_e32 v14, s9, v42
	v_add_u32_e32 v20, s9, v44
	v_add_u32_e32 v22, s9, v46
	v_add_u32_e32 v28, s9, v48
	v_add_u32_e32 v32, s9, v50
	v_mad_i64_i32 v[4:5], s[2:3], v4, s13, v[0:1]
	v_mad_i64_i32 v[8:9], s[2:3], v6, s13, v[0:1]
	v_mad_i64_i32 v[12:13], s[2:3], v12, s13, v[0:1]
	v_mad_i64_i32 v[16:17], s[2:3], v14, s13, v[0:1]
	v_mad_i64_i32 v[20:21], s[2:3], v20, s13, v[0:1]
	v_mad_i64_i32 v[24:25], s[2:3], v22, s13, v[0:1]
	v_mad_i64_i32 v[28:29], s[2:3], v28, s13, v[0:1]
	v_mad_i64_i32 v[0:1], s[2:3], v32, s13, v[0:1]
	global_load_dwordx4 v[4:7], v[4:5], off
	s_nop 0
	global_load_dwordx4 v[8:11], v[8:9], off
	s_nop 0
	global_load_dwordx4 v[12:15], v[12:13], off
	s_nop 0
	global_load_dwordx4 v[16:19], v[16:17], off
	s_nop 0
	global_load_dwordx4 v[20:23], v[20:21], off
	s_nop 0
	global_load_dwordx4 v[24:27], v[24:25], off
	v_add_u32_e32 v206, 0x11800, v205
	global_load_dwordx4 v[28:31], v[28:29], off
	v_ashrrev_i32_e32 v51, 6, v204
	global_load_dwordx4 v[32:35], v[0:1], off
	v_add_u32_e32 v0, v206, v2
	v_mad_u64_u32 v[36:37], s[10:11], v36, s30, v[0:1]
	v_mad_u64_u32 v[38:39], s[10:11], v38, s30, v[0:1]
	v_mad_u64_u32 v[40:41], s[10:11], v40, s30, v[0:1]
	v_mad_u64_u32 v[42:43], s[10:11], v42, s30, v[0:1]
	v_mad_u64_u32 v[44:45], s[10:11], v44, s30, v[0:1]
	v_mad_u64_u32 v[46:47], s[10:11], v46, s30, v[0:1]
	v_mad_u64_u32 v[48:49], s[10:11], v48, s30, v[0:1]
	v_mad_u64_u32 v[0:1], s[10:11], v50, s30, v[0:1]
	v_and_b32_e32 v2, 63, v204
	v_readfirstlane_b32 s2, v51
	s_mov_b64 s[24:25], 0x400
	v_mov_b32_e32 v226, 0x3ecc95a3
	v_mov_b32_e32 v210, 0
	v_mov_b32_e32 v208, 0xf149f2ca
	s_waitcnt vmcnt(7)
	ds_write_b128 v36, v[4:7]
	s_waitcnt vmcnt(6)
	ds_write_b128 v38, v[8:11]
	s_waitcnt vmcnt(5)
	ds_write_b128 v40, v[12:15]
	s_waitcnt vmcnt(4)
	ds_write_b128 v42, v[16:19]
	s_waitcnt vmcnt(3)
	ds_write_b128 v44, v[20:23]
	s_waitcnt vmcnt(2)
	ds_write_b128 v46, v[24:27]
	s_waitcnt vmcnt(1)
	ds_write_b128 v48, v[28:31]
	v_or_b32_e32 v4, s9, v2
	v_lshlrev_b32_e32 v2, 2, v2
	v_mov_b32_e32 v14, v3
	s_waitcnt vmcnt(0)
	ds_write_b128 v0, v[32:35]
	v_mov_b64_e32 v[0:1], s[52:53]
	v_mad_i64_i32 v[0:1], s[10:11], v4, s13, v[0:1]
	s_lshl_b32 s10, s2, 3
	s_add_i32 s11, s12, 0xffffff00
	s_cmp_lt_i32 s2, 32
	s_cselect_b32 s3, s9, s11
	s_add_i32 s3, s3, s10
	s_mul_hi_i32 s12, s3, 0x1400
	s_mulk_i32 s3, 0x1400
	s_add_u32 s3, s52, s3
	v_lshlrev_b32_e32 v4, 3, v51
	s_addc_u32 s13, s53, s12
	v_lshl_add_u64 v[0:1], v[0:1], 0, s[80:81]
	v_ashrrev_i32_e32 v5, 31, v4
	s_add_u32 s12, s3, s80
	v_lshl_add_u64 v[0:1], v[4:5], 1, v[0:1]
	s_addc_u32 s13, s13, 0
	global_load_dwordx4 v[176:179], v[0:1], off offset:2048
	global_load_dwordx4 v[180:183], v[0:1], off offset:2176
	v_lshl_add_u64 v[0:1], s[12:13], 0, v[2:3]
	s_mul_i32 s13, s2, 0x880
	v_add_u32_e32 v4, s13, v205
	s_or_b32 s14, s10, 1
	v_readfirstlane_b32 s3, v4
	s_cmpk_lt_i32 s14, 0x100
	s_mov_b32 m0, s3
	s_cselect_b32 s3, s9, s11
	s_add_i32 s3, s3, s14
	s_mul_hi_i32 s12, s3, 0x1400
	s_mulk_i32 s3, 0x1400
	s_add_u32 s3, s52, s3
	s_mulk_i32 s14, 0x110
	s_addc_u32 s12, s53, s12
	v_add_u32_e32 v4, s14, v205
	v_lshl_add_u64 v[0:1], v[0:1], 0, s[24:25]
	s_add_u32 s22, s3, s80
	v_readfirstlane_b32 s3, v4
	global_load_lds_dword v[0:1], off
	s_addc_u32 s23, s12, 0
	s_mov_b32 m0, s3
	s_or_b32 s3, s10, 2
	s_cmpk_lt_i32 s3, 0x100
	s_cselect_b32 s12, s9, s11
	s_add_i32 s3, s12, s3
	s_mul_hi_i32 s12, s3, 0x1400
	s_mulk_i32 s3, 0x1400
	s_add_u32 s3, s52, s3
	s_addc_u32 s12, s53, s12
	v_lshl_add_u64 v[0:1], s[22:23], 0, v[2:3]
	s_add_u32 s22, s3, s80
	s_addc_u32 s23, s12, 0
	s_add_i32 s3, s14, 0x110
	v_add_u32_e32 v4, s3, v205
	v_lshl_add_u64 v[0:1], v[0:1], 0, s[24:25]
	v_readfirstlane_b32 s3, v4
	global_load_lds_dword v[0:1], off
	s_mov_b32 m0, s3
	s_or_b32 s3, s10, 3
	s_cmpk_lt_i32 s3, 0x100
	s_cselect_b32 s12, s9, s11
	s_add_i32 s3, s12, s3
	s_mul_hi_i32 s12, s3, 0x1400
	s_mulk_i32 s3, 0x1400
	s_add_u32 s3, s52, s3
	s_addc_u32 s12, s53, s12
	v_lshl_add_u64 v[0:1], s[22:23], 0, v[2:3]
	s_add_u32 s22, s3, s80
	s_addc_u32 s23, s12, 0
	s_add_i32 s3, s14, 0x220
	v_add_u32_e32 v4, s3, v205
	v_lshl_add_u64 v[0:1], v[0:1], 0, s[24:25]
	v_readfirstlane_b32 s3, v4
	global_load_lds_dword v[0:1], off
	s_mov_b32 m0, s3
	s_or_b32 s3, s10, 4
	s_cmpk_lt_i32 s3, 0x100
	s_cselect_b32 s12, s9, s11
	s_add_i32 s3, s12, s3
	s_mul_hi_i32 s12, s3, 0x1400
	s_mulk_i32 s3, 0x1400
	s_add_u32 s3, s52, s3
	s_addc_u32 s12, s53, s12
	v_lshl_add_u64 v[0:1], s[22:23], 0, v[2:3]
	s_add_u32 s22, s3, s80
	s_addc_u32 s23, s12, 0
	s_add_i32 s3, s14, 0x330
	v_add_u32_e32 v4, s3, v205
	v_lshl_add_u64 v[0:1], v[0:1], 0, s[24:25]
	v_readfirstlane_b32 s3, v4
	global_load_lds_dword v[0:1], off
	s_mov_b32 m0, s3
	s_or_b32 s3, s10, 5
	s_cmpk_lt_i32 s3, 0x100
	s_cselect_b32 s12, s9, s11
	s_add_i32 s3, s12, s3
	s_mul_hi_i32 s12, s3, 0x1400
	s_mulk_i32 s3, 0x1400
	s_add_u32 s3, s52, s3
	s_addc_u32 s12, s53, s12
	v_lshl_add_u64 v[0:1], s[22:23], 0, v[2:3]
	s_add_u32 s22, s3, s80
	s_addc_u32 s23, s12, 0
	s_add_i32 s3, s14, 0x440
	v_add_u32_e32 v4, s3, v205
	v_lshl_add_u64 v[0:1], v[0:1], 0, s[24:25]
	v_readfirstlane_b32 s3, v4
	global_load_lds_dword v[0:1], off
	s_mov_b32 m0, s3
	s_or_b32 s3, s10, 6
	s_cmpk_lt_i32 s3, 0x100
	s_cselect_b32 s12, s9, s11
	s_add_i32 s3, s12, s3
	s_mul_hi_i32 s12, s3, 0x1400
	s_mulk_i32 s3, 0x1400
	s_add_u32 s3, s52, s3
	s_addc_u32 s12, s53, s12
	v_lshl_add_u64 v[0:1], s[22:23], 0, v[2:3]
	s_add_u32 s22, s3, s80
	s_addc_u32 s23, s12, 0
	s_add_i32 s3, s14, 0x550
	v_add_u32_e32 v4, s3, v205
	v_lshl_add_u64 v[0:1], v[0:1], 0, s[24:25]
	v_readfirstlane_b32 s3, v4
	global_load_lds_dword v[0:1], off
	s_mov_b32 m0, s3
	s_or_b32 s3, s10, 7
	s_cmpk_lt_i32 s3, 0x100
	s_cselect_b32 s12, s9, s11
	s_add_i32 s3, s12, s3
	s_mul_hi_i32 s12, s3, 0x1400
	s_mulk_i32 s3, 0x1400
	s_add_u32 s3, s52, s3
	s_addc_u32 s12, s53, s12
	v_lshl_add_u64 v[0:1], s[22:23], 0, v[2:3]
	s_add_u32 s22, s3, s80
	v_lshl_add_u64 v[0:1], v[0:1], 0, s[24:25]
	s_addc_u32 s23, s12, 0
	s_add_i32 s3, s14, 0x660
	global_load_lds_dword v[0:1], off
	v_lshl_add_u64 v[0:1], s[22:23], 0, v[2:3]
	v_add_u32_e32 v2, s3, v205
	v_lshl_add_u64 v[0:1], v[0:1], 0, s[24:25]
	v_readfirstlane_b32 s3, v2
	s_mov_b32 m0, s3
	s_movk_i32 s3, 0x480
	global_load_lds_dword v[0:1], off
	v_bfe_u32 v0, v204, 2, 2
	v_and_b32_e32 v1, 12, v204
	v_cmp_ne_u32_e32 vcc, 2, v0
	v_mov_b32_e32 v15, v3
	v_mov_b32_e32 v2, v3
	v_cndmask_b32_e32 v1, 4, v1, vcc
	v_cmp_ne_u32_e32 vcc, 1, v0
	v_mov_b32_e32 v4, v3
	v_mov_b32_e32 v5, v3
	v_cndmask_b32_e32 v0, 8, v1, vcc
	v_and_or_b32 v0, v204, 51, v0
	v_mul_lo_u32 v1, v51, s3
	v_lshlrev_b32_e32 v0, 1, v0
	v_add3_u32 v0, v205, v1, v0
	s_waitcnt vmcnt(0)
	ds_write_b16 v0, v176 offset:34816
	ds_write_b16_d16_hi v0, v176 offset:34960
	ds_write_b16 v0, v177 offset:35104
	ds_write_b16_d16_hi v0, v177 offset:35248
	ds_write_b16 v0, v178 offset:35392
	ds_write_b16_d16_hi v0, v178 offset:35536
	ds_write_b16 v0, v179 offset:35680
	ds_write_b16_d16_hi v0, v179 offset:35824
	ds_write_b16 v0, v180 offset:44032
	ds_write_b16_d16_hi v0, v180 offset:44176
	ds_write_b16 v0, v181 offset:44320
	ds_write_b16_d16_hi v0, v181 offset:44464
	ds_write_b16 v0, v182 offset:44608
	ds_write_b16_d16_hi v0, v182 offset:44752
	ds_write_b16 v0, v183 offset:44896
	ds_write_b16_d16_hi v0, v183 offset:45040
	v_mov_b32_e32 v0, v3
	v_mov_b32_e32 v1, v3
	v_mov_b32_e32 v6, v3
	v_mov_b32_e32 v7, v3
	v_mov_b32_e32 v8, v3
	v_mov_b32_e32 v9, v3
	v_mov_b32_e32 v10, v3
	v_mov_b32_e32 v11, v3
	v_mov_b32_e32 v12, v3
	v_mov_b32_e32 v13, v3
	v_mov_b64_e32 v[30:31], v[14:15]
	v_mov_b64_e32 v[62:63], v[14:15]
	v_mov_b64_e32 v[94:95], v[14:15]
	v_mov_b64_e32 v[126:127], v[14:15]
	v_mov_b64_e32 v[46:47], v[14:15]
	v_mov_b64_e32 v[78:79], v[14:15]
	v_mov_b64_e32 v[110:111], v[14:15]
	v_mov_b64_e32 v[142:143], v[14:15]
	s_lshl_b32 s12, s2, 5
	s_addk_i32 s15, 0x4040
	s_mov_b32 s22, 0
	v_mov_b64_e32 v[28:29], v[12:13]
	v_mov_b64_e32 v[26:27], v[10:11]
	v_mov_b64_e32 v[24:25], v[8:9]
	v_mov_b64_e32 v[22:23], v[6:7]
	v_mov_b64_e32 v[20:21], v[4:5]
	v_mov_b64_e32 v[18:19], v[2:3]
	v_mov_b64_e32 v[16:17], v[0:1]
	v_mov_b64_e32 v[60:61], v[12:13]
	v_mov_b64_e32 v[58:59], v[10:11]
	v_mov_b64_e32 v[56:57], v[8:9]
	v_mov_b64_e32 v[54:55], v[6:7]
	v_mov_b64_e32 v[52:53], v[4:5]
	v_mov_b64_e32 v[50:51], v[2:3]
	v_mov_b64_e32 v[48:49], v[0:1]
	v_mov_b64_e32 v[92:93], v[12:13]
	v_mov_b64_e32 v[90:91], v[10:11]
	v_mov_b64_e32 v[88:89], v[8:9]
	v_mov_b64_e32 v[86:87], v[6:7]
	v_mov_b64_e32 v[84:85], v[4:5]
	v_mov_b64_e32 v[82:83], v[2:3]
	v_mov_b64_e32 v[80:81], v[0:1]
	v_mov_b64_e32 v[124:125], v[12:13]
	v_mov_b64_e32 v[122:123], v[10:11]
	v_mov_b64_e32 v[120:121], v[8:9]
	v_mov_b64_e32 v[118:119], v[6:7]
	v_mov_b64_e32 v[116:117], v[4:5]
	v_mov_b64_e32 v[114:115], v[2:3]
	v_mov_b64_e32 v[112:113], v[0:1]
	v_mov_b64_e32 v[44:45], v[12:13]
	v_mov_b64_e32 v[42:43], v[10:11]
	v_mov_b64_e32 v[40:41], v[8:9]
	v_mov_b64_e32 v[38:39], v[6:7]
	v_mov_b64_e32 v[36:37], v[4:5]
	v_mov_b64_e32 v[34:35], v[2:3]
	v_mov_b64_e32 v[32:33], v[0:1]
	v_mov_b64_e32 v[76:77], v[12:13]
	v_mov_b64_e32 v[74:75], v[10:11]
	v_mov_b64_e32 v[72:73], v[8:9]
	v_mov_b64_e32 v[70:71], v[6:7]
	v_mov_b64_e32 v[68:69], v[4:5]
	v_mov_b64_e32 v[66:67], v[2:3]
	v_mov_b64_e32 v[64:65], v[0:1]
	v_mov_b64_e32 v[108:109], v[12:13]
	v_mov_b64_e32 v[106:107], v[10:11]
	v_mov_b64_e32 v[104:105], v[8:9]
	v_mov_b64_e32 v[102:103], v[6:7]
	v_mov_b64_e32 v[100:101], v[4:5]
	v_mov_b64_e32 v[98:99], v[2:3]
	v_mov_b64_e32 v[96:97], v[0:1]
	v_mov_b64_e32 v[140:141], v[12:13]
	v_mov_b64_e32 v[138:139], v[10:11]
	v_mov_b64_e32 v[136:137], v[8:9]
	v_mov_b64_e32 v[134:135], v[6:7]
	v_mov_b64_e32 v[132:133], v[4:5]
	v_mov_b64_e32 v[130:131], v[2:3]
	v_mov_b64_e32 v[128:129], v[0:1]
	v_mov_b32_e32 v209, 0xf149f2ca
	v_mov_b32_e32 v207, 0
	s_mov_b32 s25, 0
	s_waitcnt lgkmcnt(0)
	s_barrier
	v_and_b32_e32 v2, 31, v204
	v_bfe_u32 v15, v204, 5, 1
	v_lshlrev_b32_e32 v15, 4, v15
	v_or_b32_e32 v13, s12, v2
	v_mul_u32_u24_e32 v1, 0x90, v2
	v_mad_u32_u24 v0, v2, s30, v15
	v_mul_lo_u32 v13, v13, s30
	v_add_u32_e32 v0, v0, v205
	v_add3_u32 v1, v1, v15, v205
	v_add3_u32 v13, v206, v13, v15
	v_bfe_u32 v15, v204, 2, 2
	v_and_b32_e32 v2, 12, v204
	v_cmp_ne_u32_e32 vcc, 2, v15
	s_movk_i32 s24, 0x480
	v_ashrrev_i32_e32 v211, 6, v204
	v_cndmask_b32_e32 v2, 4, v2, vcc
	v_cmp_ne_u32_e32 vcc, 1, v15
	v_mul_lo_u32 v211, v211, s24
	s_nop 0
	v_cndmask_b32_e32 v15, 8, v2, vcc
	v_and_or_b32 v2, v204, 51, v15
	v_lshlrev_b32_e32 v2, 1, v2
	v_add3_u32 v2, v205, v211, v2
	v_and_b32_e32 v206, 63, v204
	v_ashrrev_i32_e32 v252, 6, v204
	s_movk_i32 s24, 0x1400
	v_lshlrev_b32_e32 v252, 4, v252
	v_mad_u32_u24 v252, v206, s24, v252
	v_lshlrev_b32_e32 v206, 2, v206
	v_add_u32_e32 v206, 0x400, v206
.LBB0_747:
	s_add_i32 s23, s25, 1
	s_and_b32 s27, s25, 1
	s_mul_i32 s26, s27, 0x4400
	s_mul_i32 s31, s27, 0x4800
	v_add_u32_e32 v12, s26, v0
	v_add_u32_e32 v14, s31, v1
	ds_read_b128 v[228:231], v12 offset:0
	ds_read_b128 v[232:235], v12 offset:32
	ds_read_b128 v[236:239], v12 offset:64
	ds_read_b128 v[240:243], v12 offset:96
	ds_read_b128 v[244:247], v13 offset:0
	ds_read_b128 v[248:251], v13 offset:32
	ds_read_b128 v[4:7], v13 offset:64
	ds_read_b128 v[8:11], v13 offset:96
	ds_read_b128 v[184:187], v14 offset:34816
	ds_read_b128 v[188:191], v14 offset:39424
	ds_read_b128 v[192:195], v14 offset:44032
	ds_read_b128 v[196:199], v14 offset:48640
	ds_read_b128 v[200:203], v14 offset:34848
	ds_read_b128 v[212:215], v14 offset:39456
	ds_read_b128 v[216:219], v14 offset:44064
	s_cmp_gt_u32 s25, 2
	s_waitcnt lgkmcnt(7)
	ds_read_b128 v[220:223], v14 offset:48672
	s_cbranch_scc1 .Lat2_noload
	v_mfma_f32_32x32x16_bf16 v[144:159], v[228:231], v[244:247], 0
	s_mov_b32 s26, s15
	s_mov_b32 s31, s9
	s_add_i32 s26, s26, s22
	s_add_i32 s31, s31, s10
	s_mul_hi_i32 s37, s26, 0x1400
	s_mul_i32 s36, s26, 0x1400
	s_add_i32 s31, s31, s22
	s_add_u32 s36, s0, s36
	s_addc_u32 s37, s1, s37
	s_add_i32 s31, s31, 64
	global_load_dwordx4 v[176:179], v252, s[36:37] offset:2048
	global_load_dwordx4 v[180:183], v252, s[36:37] offset:2176
	s_mul_hi_i32 s37, s31, 0x1400
	s_mul_i32 s36, s31, 0x1400
	s_add_u32 s36, s0, s36
	v_mfma_f32_32x32x16_bf16 v[144:159], v[232:235], v[248:251], v[144:159]
	s_addc_u32 s37, s1, s37
	v_readfirstlane_b32 s2, v205
	s_xor_b32 s3, s27, 1
	s_mul_i32 s3, s3, 0x4400
	s_add_i32 s2, s2, s13
	s_add_i32 s2, s2, s3
	s_add_i32 m0, s2, 0
	s_nop 0
	global_load_lds_dword v206, s[36:37]
	s_add_u32 s36, s36, 0x1400
	s_addc_u32 s37, s37, 0
	s_add_i32 m0, s2, 272
	s_nop 0
	global_load_lds_dword v206, s[36:37]
	s_add_u32 s36, s36, 0x1400
	v_mfma_f32_32x32x16_bf16 v[144:159], v[236:239], v[4:7], v[144:159]
	s_addc_u32 s37, s37, 0
	s_add_i32 m0, s2, 544
	s_nop 0
	global_load_lds_dword v206, s[36:37]
	s_add_u32 s36, s36, 0x1400
	s_addc_u32 s37, s37, 0
	s_add_i32 m0, s2, 816
	s_nop 0
	global_load_lds_dword v206, s[36:37]
	s_add_u32 s36, s36, 0x1400
	s_addc_u32 s37, s37, 0
	s_add_i32 m0, s2, 1088
	s_nop 0
	global_load_lds_dword v206, s[36:37]
	s_add_u32 s36, s36, 0x1400
	v_mfma_f32_32x32x16_bf16 v[144:159], v[240:243], v[8:11], v[144:159]
	s_addc_u32 s37, s37, 0
	s_add_i32 m0, s2, 1360
	s_nop 0
	global_load_lds_dword v206, s[36:37]
	s_add_u32 s36, s36, 0x1400
	s_addc_u32 s37, s37, 0
	s_add_i32 m0, s2, 1632
	s_nop 0
	global_load_lds_dword v206, s[36:37]
	s_add_u32 s36, s36, 0x1400
	s_addc_u32 s37, s37, 0
	s_add_i32 m0, s2, 1904
	s_nop 0
	global_load_lds_dword v206, s[36:37]
	s_branch .Lat2_join
